# strategy 4: static s_setprio 1 for waves 4-7 at the start of every non-GEMM phase (on top of best)
# speedup vs baseline: 1.0050x; 1.0003x over previous
.LBB0_105:
	v_readfirstlane_b32 s32, v0
	s_cmp_lt_u32 s32, 0x100
	s_cbranch_scc1 .Lprio_p1
	s_setprio 1
